# expert GEMM epilogues: dropped the 32-wait-state pad before the accumulator reads (70+ instructions and LDS waits already separate them)
# speedup vs baseline: 1.0042x; 1.0042x over previous
.LBB0_1916:
	s_mov_b32 s29, 0
	v_mov_b32_e32 v4, v166
	v_mov_b32_e32 v2, v167
	v_mov_b32_e32 v3, s24
	s_add_u32 s40, s2, 0xffffff00
	ds_read_b32 v3, v3 offset:288
	s_addc_u32 s41, s23, -1
	s_lshl_b32 s2, s31, 11
	s_add_i32 s2, s2, 0
	v_lshl_add_u32 v18, v2, 3, s83
	s_add_i32 s2, s2, 0x21000
	v_lshl_add_u32 v5, v18, 3, s2
	ds_read_b128 v[14:17], v5
	s_waitcnt lgkmcnt(1)
	v_readfirstlane_b32 s8, v3
	s_lshl_b32 s8, s8, 2
	s_add_i32 s8, s8, 0
	s_add_i32 s8, s8, 0x201c0
	v_mov_b32_e32 v2, s8
	ds_read2_b32 v[2:3], v2 offset1:32
	v_add_u32_e32 v19, s82, v4
	ds_read_b128 v[10:13], v5 offset:16
	ds_read_b128 v[6:9], v5 offset:32
	v_add_u32_e32 v22, 16, v19
	v_add_u32_e32 v24, 32, v19
	s_waitcnt lgkmcnt(2)
	v_readfirstlane_b32 s9, v2
	v_lshl_add_u32 v2, v19, 2, s2
	ds_read_b32 v20, v2 offset:1024
	v_readfirstlane_b32 s8, v3
	s_sub_i32 s8, s36, s8
	v_lshl_add_u32 v23, v22, 2, s2
	v_lshl_add_u32 v25, v24, 2, s2
	s_lshl_b32 s8, s8, 8
	ds_read_b128 v[2:5], v5 offset:48
	ds_read_b32 v23, v23 offset:1024
	ds_read_b32 v25, v25 offset:1024
	v_add_u32_e32 v21, s8, v19
	s_waitcnt lgkmcnt(3)
	v_mul_f32_e32 v20, 0x3b800000, v20
	v_cmp_gt_i32_e32 vcc, s9, v21
	s_waitcnt lgkmcnt(1)
	v_mul_f32_e32 v21, 0x3b800000, v23
	v_add_u32_e32 v26, 0xa0, v19
	v_cndmask_b32_e32 v180, 0, v20, vcc
	v_add_u32_e32 v20, s8, v22
	v_cmp_gt_i32_e32 vcc, s9, v20
	v_add_u32_e32 v20, s8, v24
	v_add_u32_e32 v22, 0x80, v19
	v_cndmask_b32_e32 v164, 0, v21, vcc
	s_waitcnt lgkmcnt(0)
	v_mul_f32_e32 v21, 0x3b800000, v25
	v_cmp_gt_i32_e32 vcc, s9, v20
	v_add_u32_e32 v20, 48, v19
	v_add_u32_e32 v24, 0x90, v19
	v_cndmask_b32_e32 v162, 0, v21, vcc
	v_lshl_add_u32 v21, v20, 2, s2
	v_lshl_add_u32 v23, v22, 2, s2
	v_lshl_add_u32 v25, v24, 2, s2
	v_lshl_add_u32 v27, v26, 2, s2
	v_add_u32_e32 v29, 0xb0, v19
	v_add_u32_e32 v20, s8, v20
	v_lshl_add_u32 v28, v29, 2, s2
	ds_read_b32 v21, v21 offset:1024
	ds_read_b32 v23, v23 offset:1024
	ds_read_b32 v25, v25 offset:1024
	ds_read_b32 v27, v27 offset:1024
	ds_read_b32 v31, v28 offset:1024
	s_waitcnt lgkmcnt(4)
	v_mul_f32_e32 v21, 0x3b800000, v21
	v_cmp_gt_i32_e32 vcc, s9, v20
	v_add_u32_e32 v20, s8, v22
	s_lshl_b32 s42, s14, 7
	v_cndmask_b32_e32 v32, 0, v21, vcc
	s_waitcnt lgkmcnt(3)
	v_mul_f32_e32 v21, 0x3b800000, v23
	v_cmp_gt_i32_e32 vcc, s9, v20
	v_add_u32_e32 v20, s8, v24
	v_mov_b32_e32 v24, v14
	v_cndmask_b32_e32 v30, 0, v21, vcc
	s_waitcnt lgkmcnt(2)
	v_mul_f32_e32 v21, 0x3b800000, v25
	v_mov_b32_e32 v25, v16
	v_pk_fma_f32 v[182:183], v[158:159], v[180:181], v[24:25] op_sel_hi:[1,0,1]
	v_mov_b32_e32 v16, v15
	v_min_f32_e32 v182, 0x40e00000, v182
	v_min_f32_e32 v183, 0x40e00000, v183
	v_pk_mul_f32 v[184:185], v[182:183], s[20:21] op_sel_hi:[1,0]
	v_cmp_gt_i32_e32 vcc, s9, v20
	v_exp_f32_e32 v184, v184
	v_exp_f32_e32 v185, v185
	v_add_u32_e32 v20, s8, v26
	v_cndmask_b32_e32 v28, 0, v21, vcc
	s_waitcnt lgkmcnt(1)
	v_mul_f32_e32 v21, 0x3b800000, v27
	v_pk_add_f32 v[14:15], v[184:185], 1.0 op_sel_hi:[1,0]
	v_pk_fma_f32 v[184:185], v[126:127], v[180:181], v[16:17] op_sel_hi:[1,0,1]
	v_rcp_f32_e32 v14, v14
	v_rcp_f32_e32 v15, v15
	v_med3_f32 v184, v184, s37, v176
	v_med3_f32 v185, v185, s37, v176
	v_cmp_gt_i32_e32 vcc, s9, v20
	v_pk_mul_f32 v[14:15], v[182:183], v[14:15]
	v_add_u32_e32 v20, s8, v29
	v_pk_fma_f32 v[182:183], v[184:185], v[14:15], v[14:15]
	v_mov_b32_e32 v14, v10
	v_mov_b32_e32 v15, v12
	v_pk_fma_f32 v[184:185], v[160:161], v[180:181], v[14:15] op_sel_hi:[1,0,1]
	v_mov_b32_e32 v12, v11
	v_min_f32_e32 v184, 0x40e00000, v184
	v_min_f32_e32 v185, 0x40e00000, v185
	v_pk_mul_f32 v[186:187], v[184:185], s[20:21] op_sel_hi:[1,0]
	v_cndmask_b32_e32 v26, 0, v21, vcc
	v_exp_f32_e32 v186, v186
	v_exp_f32_e32 v187, v187
	s_waitcnt lgkmcnt(0)
	v_mul_f32_e32 v21, 0x3b800000, v31
	v_cmp_gt_i32_e32 vcc, s9, v20
	v_pk_add_f32 v[10:11], v[186:187], 1.0 op_sel_hi:[1,0]
	v_cndmask_b32_e32 v22, 0, v21, vcc
	v_rcp_f32_e32 v10, v10
	v_rcp_f32_e32 v11, v11
	v_cvt_pk_fp8_f32 v21, v182, v183
	v_pk_fma_f32 v[182:183], v[128:129], v[180:181], v[12:13] op_sel_hi:[1,0,1]
	v_pk_mul_f32 v[10:11], v[184:185], v[10:11]
	v_med3_f32 v182, v182, s37, v176
	v_med3_f32 v183, v183, s37, v176
	v_pk_fma_f32 v[182:183], v[182:183], v[10:11], v[10:11]
	v_mov_b32_e32 v10, v6
	v_mov_b32_e32 v11, v8
	v_pk_fma_f32 v[184:185], v[154:155], v[180:181], v[10:11] op_sel_hi:[1,0,1]
	v_mov_b32_e32 v8, v7
	v_min_f32_e32 v184, 0x40e00000, v184
	v_min_f32_e32 v185, 0x40e00000, v185
	v_pk_mul_f32 v[186:187], v[184:185], s[20:21] op_sel_hi:[1,0]
	v_cvt_pk_fp8_f32 v21, v182, v183 op_sel:[0,0,1]
	v_exp_f32_e32 v186, v186
	v_exp_f32_e32 v187, v187
	v_pk_fma_f32 v[182:183], v[122:123], v[180:181], v[8:9] op_sel_hi:[1,0,1]
	v_med3_f32 v182, v182, s37, v176
	v_pk_add_f32 v[6:7], v[186:187], 1.0 op_sel_hi:[1,0]
	v_med3_f32 v183, v183, s37, v176
	v_rcp_f32_e32 v6, v6
	v_rcp_f32_e32 v7, v7
	v_lshl_add_u32 v20, s36, 8, v19
	s_ashr_i32 s43, s42, 31
	v_pk_mul_f32 v[6:7], v[184:185], v[6:7]
	v_ashrrev_i32_e32 v19, 31, v18
	v_pk_fma_f32 v[182:183], v[182:183], v[6:7], v[6:7]
	v_mov_b32_e32 v6, v2
	v_mov_b32_e32 v7, v4
	v_pk_fma_f32 v[184:185], v[156:157], v[180:181], v[6:7] op_sel_hi:[1,0,1]
	v_mov_b32_e32 v4, v3
	v_min_f32_e32 v184, 0x40e00000, v184
	v_min_f32_e32 v185, 0x40e00000, v185
	v_pk_mul_f32 v[186:187], v[184:185], s[20:21] op_sel_hi:[1,0]
	v_pk_fma_f32 v[180:181], v[124:125], v[180:181], v[4:5] op_sel_hi:[1,0,1]
	v_exp_f32_e32 v186, v186
	v_exp_f32_e32 v187, v187
	v_cvt_pk_fp8_f32 v27, v182, v183
	v_med3_f32 v180, v180, s37, v176
	v_med3_f32 v181, v181, s37, v176
	v_pk_add_f32 v[2:3], v[186:187], 1.0 op_sel_hi:[1,0]
	v_pk_fma_f32 v[182:183], v[150:151], v[164:165], v[24:25] op_sel_hi:[1,0,1]
	v_rcp_f32_e32 v2, v2
	v_rcp_f32_e32 v3, v3
	v_min_f32_e32 v182, 0x40e00000, v182
	v_min_f32_e32 v183, 0x40e00000, v183
	s_and_b64 vcc, exec, s[6:7]
	v_pk_mul_f32 v[2:3], v[184:185], v[2:3]
	v_pk_mul_f32 v[184:185], v[182:183], s[20:21] op_sel_hi:[1,0]
	v_pk_fma_f32 v[2:3], v[180:181], v[2:3], v[2:3]
	v_exp_f32_e32 v184, v184
	v_cvt_pk_fp8_f32 v27, v2, v3 op_sel:[0,0,1]
	v_mov_b32_e32 v2, v21
	v_ashrrev_i32_e32 v21, 31, v20
	v_lshlrev_b64 v[180:181], 10, v[20:21]
	v_exp_f32_e32 v185, v185
	v_lshl_add_u64 v[180:181], s[12:13], 0, v[180:181]
	v_mov_b32_e32 v3, v27
	v_lshl_add_u64 v[180:181], v[180:181], 0, s[42:43]
	v_lshl_add_u64 v[188:189], v[180:181], 0, v[18:19]
	global_store_dwordx2 v[188:189], v[2:3], off
	v_pk_add_f32 v[2:3], v[184:185], 1.0 op_sel_hi:[1,0]
	v_pk_fma_f32 v[180:181], v[118:119], v[164:165], v[16:17] op_sel_hi:[1,0,1]
	v_rcp_f32_e32 v2, v2
	v_rcp_f32_e32 v3, v3
	v_med3_f32 v180, v180, s37, v176
	v_med3_f32 v181, v181, s37, v176
	v_pk_mul_f32 v[2:3], v[182:183], v[2:3]
	v_pk_fma_f32 v[182:183], v[152:153], v[164:165], v[14:15] op_sel_hi:[1,0,1]
	v_pk_fma_f32 v[2:3], v[180:181], v[2:3], v[2:3]
	v_min_f32_e32 v182, 0x40e00000, v182
	v_min_f32_e32 v183, 0x40e00000, v183
	v_pk_mul_f32 v[184:185], v[182:183], s[20:21] op_sel_hi:[1,0]
	v_cvt_pk_fp8_f32 v21, v2, v3
	v_exp_f32_e32 v184, v184
	v_exp_f32_e32 v185, v185
	v_pk_fma_f32 v[180:181], v[120:121], v[164:165], v[12:13] op_sel_hi:[1,0,1]
	v_med3_f32 v180, v180, s37, v176
	v_pk_add_f32 v[2:3], v[184:185], 1.0 op_sel_hi:[1,0]
	v_med3_f32 v181, v181, s37, v176
	v_rcp_f32_e32 v2, v2
	v_rcp_f32_e32 v3, v3
	s_nop 0
	v_pk_mul_f32 v[2:3], v[182:183], v[2:3]
	v_pk_fma_f32 v[182:183], v[146:147], v[164:165], v[10:11] op_sel_hi:[1,0,1]
	v_pk_fma_f32 v[2:3], v[180:181], v[2:3], v[2:3]
	v_min_f32_e32 v182, 0x40e00000, v182
	v_min_f32_e32 v183, 0x40e00000, v183
	v_pk_mul_f32 v[184:185], v[182:183], s[20:21] op_sel_hi:[1,0]
	v_cvt_pk_fp8_f32 v21, v2, v3 op_sel:[0,0,1]
	v_exp_f32_e32 v184, v184
	v_exp_f32_e32 v185, v185
	v_pk_fma_f32 v[180:181], v[114:115], v[164:165], v[8:9] op_sel_hi:[1,0,1]
	v_pk_add_f32 v[2:3], v[184:185], 1.0 op_sel_hi:[1,0]
	s_nop 0
	v_rcp_f32_e32 v2, v2
	v_rcp_f32_e32 v3, v3
	v_med3_f32 v180, v180, s37, v176
	v_med3_f32 v181, v181, s37, v176
	v_pk_mul_f32 v[2:3], v[182:183], v[2:3]
	v_pk_fma_f32 v[182:183], v[148:149], v[164:165], v[6:7] op_sel_hi:[1,0,1]
	v_pk_fma_f32 v[2:3], v[180:181], v[2:3], v[2:3]
	v_min_f32_e32 v182, 0x40e00000, v182
	v_min_f32_e32 v183, 0x40e00000, v183
	v_pk_mul_f32 v[184:185], v[182:183], s[20:21] op_sel_hi:[1,0]
	v_cvt_pk_fp8_f32 v27, v2, v3
	v_exp_f32_e32 v184, v184
	v_exp_f32_e32 v185, v185
	v_pk_fma_f32 v[180:181], v[116:117], v[164:165], v[4:5] op_sel_hi:[1,0,1]
	v_pk_add_f32 v[2:3], v[184:185], 1.0 op_sel_hi:[1,0]
	s_nop 0
	v_rcp_f32_e32 v2, v2
	v_rcp_f32_e32 v3, v3
	v_med3_f32 v180, v180, s37, v176
	v_med3_f32 v181, v181, s37, v176
	v_pk_mul_f32 v[2:3], v[182:183], v[2:3]
	v_pk_fma_f32 v[182:183], v[142:143], v[162:163], v[24:25] op_sel_hi:[1,0,1]
	v_pk_fma_f32 v[2:3], v[180:181], v[2:3], v[2:3]
	v_min_f32_e32 v182, 0x40e00000, v182
	v_min_f32_e32 v183, 0x40e00000, v183
	v_cvt_pk_fp8_f32 v27, v2, v3 op_sel:[0,0,1]
	v_pk_mul_f32 v[184:185], v[182:183], s[20:21] op_sel_hi:[1,0]
	v_exp_f32_e32 v184, v184
	v_exp_f32_e32 v185, v185
	v_mov_b32_e32 v2, v21
	v_mov_b32_e32 v3, v27
	s_mov_b32 s28, 0x4000
	v_lshl_add_u64 v[180:181], v[188:189], 0, s[28:29]
	global_store_dwordx2 v[180:181], v[2:3], off
	v_pk_add_f32 v[2:3], v[184:185], 1.0 op_sel_hi:[1,0]
	v_pk_fma_f32 v[180:181], v[110:111], v[162:163], v[16:17] op_sel_hi:[1,0,1]
	v_rcp_f32_e32 v2, v2
	v_rcp_f32_e32 v3, v3
	v_med3_f32 v180, v180, s37, v176
	v_med3_f32 v181, v181, s37, v176
	v_pk_mul_f32 v[2:3], v[182:183], v[2:3]
	v_pk_fma_f32 v[182:183], v[144:145], v[162:163], v[14:15] op_sel_hi:[1,0,1]
	v_pk_fma_f32 v[2:3], v[180:181], v[2:3], v[2:3]
	v_min_f32_e32 v182, 0x40e00000, v182
	v_min_f32_e32 v183, 0x40e00000, v183
	v_pk_mul_f32 v[184:185], v[182:183], s[20:21] op_sel_hi:[1,0]
	v_cvt_pk_fp8_f32 v21, v2, v3
	v_exp_f32_e32 v184, v184
	v_exp_f32_e32 v185, v185
	v_pk_fma_f32 v[180:181], v[112:113], v[162:163], v[12:13] op_sel_hi:[1,0,1]
	v_med3_f32 v180, v180, s37, v176
	v_pk_add_f32 v[2:3], v[184:185], 1.0 op_sel_hi:[1,0]
	v_med3_f32 v181, v181, s37, v176
	v_rcp_f32_e32 v2, v2
	v_rcp_f32_e32 v3, v3
	s_nop 0
	v_pk_mul_f32 v[2:3], v[182:183], v[2:3]
	v_pk_fma_f32 v[182:183], v[138:139], v[162:163], v[10:11] op_sel_hi:[1,0,1]
	v_pk_fma_f32 v[2:3], v[180:181], v[2:3], v[2:3]
	v_min_f32_e32 v182, 0x40e00000, v182
	v_min_f32_e32 v183, 0x40e00000, v183
	v_pk_mul_f32 v[184:185], v[182:183], s[20:21] op_sel_hi:[1,0]
	v_cvt_pk_fp8_f32 v21, v2, v3 op_sel:[0,0,1]
	v_exp_f32_e32 v184, v184
	v_exp_f32_e32 v185, v185
	v_pk_fma_f32 v[180:181], v[106:107], v[162:163], v[8:9] op_sel_hi:[1,0,1]
	v_pk_add_f32 v[2:3], v[184:185], 1.0 op_sel_hi:[1,0]
	s_nop 0
	v_rcp_f32_e32 v2, v2
	v_rcp_f32_e32 v3, v3
	v_med3_f32 v180, v180, s37, v176
	v_med3_f32 v181, v181, s37, v176
	v_pk_mul_f32 v[2:3], v[182:183], v[2:3]
	v_pk_fma_f32 v[182:183], v[140:141], v[162:163], v[6:7] op_sel_hi:[1,0,1]
	v_pk_fma_f32 v[2:3], v[180:181], v[2:3], v[2:3]
	v_min_f32_e32 v182, 0x40e00000, v182
	v_min_f32_e32 v183, 0x40e00000, v183
	v_pk_mul_f32 v[184:185], v[182:183], s[20:21] op_sel_hi:[1,0]
	v_cvt_pk_fp8_f32 v27, v2, v3
	v_exp_f32_e32 v184, v184
	v_exp_f32_e32 v185, v185
	v_pk_fma_f32 v[180:181], v[108:109], v[162:163], v[4:5] op_sel_hi:[1,0,1]
	v_pk_add_f32 v[2:3], v[184:185], 1.0 op_sel_hi:[1,0]
	s_nop 0
	v_rcp_f32_e32 v2, v2
	v_rcp_f32_e32 v3, v3
	v_med3_f32 v180, v180, s37, v176
	v_med3_f32 v181, v181, s37, v176
	v_pk_mul_f32 v[2:3], v[182:183], v[2:3]
	v_pk_fma_f32 v[182:183], v[134:135], v[32:33], v[24:25] op_sel_hi:[1,0,1]
	v_pk_fma_f32 v[2:3], v[180:181], v[2:3], v[2:3]
	v_min_f32_e32 v182, 0x40e00000, v182
	v_min_f32_e32 v183, 0x40e00000, v183
	v_cvt_pk_fp8_f32 v27, v2, v3 op_sel:[0,0,1]
	v_pk_mul_f32 v[184:185], v[182:183], s[20:21] op_sel_hi:[1,0]
	v_exp_f32_e32 v184, v184
	v_exp_f32_e32 v185, v185
	v_mov_b32_e32 v2, v21
	v_mov_b32_e32 v3, v27
	s_mov_b32 s28, 0x8000
	v_lshl_add_u64 v[180:181], v[188:189], 0, s[28:29]
	global_store_dwordx2 v[180:181], v[2:3], off
	v_pk_add_f32 v[2:3], v[184:185], 1.0 op_sel_hi:[1,0]
	v_pk_fma_f32 v[180:181], v[102:103], v[32:33], v[16:17] op_sel_hi:[1,0,1]
	v_rcp_f32_e32 v2, v2
	v_rcp_f32_e32 v3, v3
	v_med3_f32 v180, v180, s37, v176
	v_med3_f32 v181, v181, s37, v176
	v_pk_mul_f32 v[2:3], v[182:183], v[2:3]
	v_pk_fma_f32 v[182:183], v[136:137], v[32:33], v[14:15] op_sel_hi:[1,0,1]
	v_pk_fma_f32 v[2:3], v[180:181], v[2:3], v[2:3]
	v_min_f32_e32 v182, 0x40e00000, v182
	v_min_f32_e32 v183, 0x40e00000, v183
	v_pk_mul_f32 v[184:185], v[182:183], s[20:21] op_sel_hi:[1,0]
	v_cvt_pk_fp8_f32 v21, v2, v3
	v_exp_f32_e32 v184, v184
	v_exp_f32_e32 v185, v185
	v_pk_fma_f32 v[180:181], v[104:105], v[32:33], v[12:13] op_sel_hi:[1,0,1]
	v_med3_f32 v180, v180, s37, v176
	v_pk_add_f32 v[2:3], v[184:185], 1.0 op_sel_hi:[1,0]
	v_med3_f32 v181, v181, s37, v176
	v_rcp_f32_e32 v2, v2
	v_rcp_f32_e32 v3, v3
	s_nop 0
	v_pk_mul_f32 v[2:3], v[182:183], v[2:3]
	v_pk_fma_f32 v[182:183], v[130:131], v[32:33], v[10:11] op_sel_hi:[1,0,1]
	v_pk_fma_f32 v[2:3], v[180:181], v[2:3], v[2:3]
	v_min_f32_e32 v182, 0x40e00000, v182
	v_min_f32_e32 v183, 0x40e00000, v183
	v_pk_mul_f32 v[184:185], v[182:183], s[20:21] op_sel_hi:[1,0]
	v_cvt_pk_fp8_f32 v21, v2, v3 op_sel:[0,0,1]
	v_exp_f32_e32 v184, v184
	v_exp_f32_e32 v185, v185
	v_pk_fma_f32 v[180:181], v[98:99], v[32:33], v[8:9] op_sel_hi:[1,0,1]
	v_pk_add_f32 v[2:3], v[184:185], 1.0 op_sel_hi:[1,0]
	s_nop 0
	v_rcp_f32_e32 v2, v2
	v_rcp_f32_e32 v3, v3
	v_med3_f32 v180, v180, s37, v176
	v_med3_f32 v181, v181, s37, v176
	v_pk_mul_f32 v[2:3], v[182:183], v[2:3]
	v_pk_fma_f32 v[182:183], v[132:133], v[32:33], v[6:7] op_sel_hi:[1,0,1]
	v_pk_fma_f32 v[2:3], v[180:181], v[2:3], v[2:3]
	v_min_f32_e32 v182, 0x40e00000, v182
	v_min_f32_e32 v183, 0x40e00000, v183
	v_pk_mul_f32 v[184:185], v[182:183], s[20:21] op_sel_hi:[1,0]
	v_cvt_pk_fp8_f32 v27, v2, v3
	v_exp_f32_e32 v184, v184
	v_exp_f32_e32 v185, v185
	v_pk_fma_f32 v[32:33], v[100:101], v[32:33], v[4:5] op_sel_hi:[1,0,1]
	v_pk_fma_f32 v[180:181], v[94:95], v[30:31], v[24:25] op_sel_hi:[1,0,1]
	v_med3_f32 v32, v32, s37, v176
	v_pk_add_f32 v[2:3], v[184:185], 1.0 op_sel_hi:[1,0]
	v_med3_f32 v33, v33, s37, v176
	v_rcp_f32_e32 v2, v2
	v_rcp_f32_e32 v3, v3
	v_min_f32_e32 v180, 0x40e00000, v180
	v_min_f32_e32 v181, 0x40e00000, v181
	v_pk_mul_f32 v[2:3], v[182:183], v[2:3]
	s_nop 0
	v_pk_fma_f32 v[2:3], v[32:33], v[2:3], v[2:3]
	v_cvt_pk_fp8_f32 v27, v2, v3 op_sel:[0,0,1]
	v_pk_mul_f32 v[182:183], v[180:181], s[20:21] op_sel_hi:[1,0]
	v_exp_f32_e32 v182, v182
	v_exp_f32_e32 v183, v183
	v_mov_b32_e32 v2, v21
	v_mov_b32_e32 v3, v27
	s_mov_b32 s28, 0xc000
	v_lshl_add_u64 v[32:33], v[188:189], 0, s[28:29]
	global_store_dwordx2 v[32:33], v[2:3], off
	v_pk_add_f32 v[32:33], v[182:183], 1.0 op_sel_hi:[1,0]
	v_pk_fma_f32 v[182:183], v[62:63], v[30:31], v[16:17] op_sel_hi:[1,0,1]
	v_rcp_f32_e32 v32, v32
	v_rcp_f32_e32 v33, v33
	v_med3_f32 v182, v182, s37, v176
	v_med3_f32 v183, v183, s37, v176
	v_pk_mul_f32 v[32:33], v[180:181], v[32:33]
	v_pk_fma_f32 v[180:181], v[96:97], v[30:31], v[14:15] op_sel_hi:[1,0,1]
	v_pk_fma_f32 v[32:33], v[182:183], v[32:33], v[32:33]
	v_min_f32_e32 v180, 0x40e00000, v180
	v_min_f32_e32 v181, 0x40e00000, v181
	v_pk_mul_f32 v[184:185], v[180:181], s[20:21] op_sel_hi:[1,0]
	v_cvt_pk_fp8_f32 v3, v32, v33
	v_exp_f32_e32 v184, v184
	v_exp_f32_e32 v185, v185
	v_pk_fma_f32 v[182:183], v[64:65], v[30:31], v[12:13] op_sel_hi:[1,0,1]
	v_med3_f32 v182, v182, s37, v176
	v_pk_add_f32 v[32:33], v[184:185], 1.0 op_sel_hi:[1,0]
	v_med3_f32 v183, v183, s37, v176
	v_rcp_f32_e32 v32, v32
	v_rcp_f32_e32 v33, v33
	s_nop 0
	v_pk_mul_f32 v[32:33], v[180:181], v[32:33]
	v_pk_fma_f32 v[180:181], v[90:91], v[30:31], v[10:11] op_sel_hi:[1,0,1]
	v_pk_fma_f32 v[32:33], v[182:183], v[32:33], v[32:33]
	v_min_f32_e32 v180, 0x40e00000, v180
	v_min_f32_e32 v181, 0x40e00000, v181
	v_pk_mul_f32 v[184:185], v[180:181], s[20:21] op_sel_hi:[1,0]
	v_cvt_pk_fp8_f32 v3, v32, v33 op_sel:[0,0,1]
	v_exp_f32_e32 v184, v184
	v_exp_f32_e32 v185, v185
	v_pk_fma_f32 v[182:183], v[58:59], v[30:31], v[8:9] op_sel_hi:[1,0,1]
	v_med3_f32 v182, v182, s37, v176
	v_pk_add_f32 v[32:33], v[184:185], 1.0 op_sel_hi:[1,0]
	v_med3_f32 v183, v183, s37, v176
	v_rcp_f32_e32 v32, v32
	v_rcp_f32_e32 v33, v33
	s_nop 0
	v_pk_mul_f32 v[32:33], v[180:181], v[32:33]
	v_pk_fma_f32 v[180:181], v[92:93], v[30:31], v[6:7] op_sel_hi:[1,0,1]
	v_pk_fma_f32 v[32:33], v[182:183], v[32:33], v[32:33]
	v_min_f32_e32 v180, 0x40e00000, v180
	v_min_f32_e32 v181, 0x40e00000, v181
	v_pk_mul_f32 v[184:185], v[180:181], s[20:21] op_sel_hi:[1,0]
	v_cvt_pk_fp8_f32 v23, v32, v33
	v_exp_f32_e32 v184, v184
	v_exp_f32_e32 v185, v185
	v_pk_fma_f32 v[30:31], v[60:61], v[30:31], v[4:5] op_sel_hi:[1,0,1]
	v_med3_f32 v30, v30, s37, v176
	v_pk_add_f32 v[32:33], v[184:185], 1.0 op_sel_hi:[1,0]
	v_med3_f32 v31, v31, s37, v176
	v_rcp_f32_e32 v32, v32
	v_rcp_f32_e32 v33, v33
	s_nop 0
	v_pk_mul_f32 v[32:33], v[180:181], v[32:33]
	s_nop 0
	v_pk_fma_f32 v[30:31], v[30:31], v[32:33], v[32:33]
	v_pk_fma_f32 v[32:33], v[86:87], v[28:29], v[24:25] op_sel_hi:[1,0,1]
	v_cvt_pk_fp8_f32 v23, v30, v31 op_sel:[0,0,1]
	v_min_f32_e32 v32, 0x40e00000, v32
	v_min_f32_e32 v33, 0x40e00000, v33
	v_mov_b32_e32 v30, v3
	v_pk_mul_f32 v[180:181], v[32:33], s[20:21] op_sel_hi:[1,0]
	v_exp_f32_e32 v180, v180
	v_exp_f32_e32 v181, v181
	v_mov_b32_e32 v31, v23
	s_mov_b32 s28, 0x20000
	v_lshl_add_u64 v[2:3], v[188:189], 0, s[28:29]
	global_store_dwordx2 v[2:3], v[30:31], off
	v_pk_add_f32 v[2:3], v[180:181], 1.0 op_sel_hi:[1,0]
	v_pk_fma_f32 v[30:31], v[54:55], v[28:29], v[16:17] op_sel_hi:[1,0,1]
	v_rcp_f32_e32 v2, v2
	v_rcp_f32_e32 v3, v3
	v_med3_f32 v30, v30, s37, v176
	v_med3_f32 v31, v31, s37, v176
	v_pk_mul_f32 v[2:3], v[32:33], v[2:3]
	v_pk_fma_f32 v[32:33], v[88:89], v[28:29], v[14:15] op_sel_hi:[1,0,1]
	v_pk_fma_f32 v[2:3], v[30:31], v[2:3], v[2:3]
	v_min_f32_e32 v32, 0x40e00000, v32
	v_min_f32_e32 v33, 0x40e00000, v33
	v_pk_mul_f32 v[180:181], v[32:33], s[20:21] op_sel_hi:[1,0]
	v_cvt_pk_fp8_f32 v21, v2, v3
	v_exp_f32_e32 v180, v180
	v_exp_f32_e32 v181, v181
	v_pk_fma_f32 v[30:31], v[56:57], v[28:29], v[12:13] op_sel_hi:[1,0,1]
	v_med3_f32 v30, v30, s37, v176
	v_pk_add_f32 v[2:3], v[180:181], 1.0 op_sel_hi:[1,0]
	v_med3_f32 v31, v31, s37, v176
	v_rcp_f32_e32 v2, v2
	v_rcp_f32_e32 v3, v3
	s_nop 0
	v_pk_mul_f32 v[2:3], v[32:33], v[2:3]
	v_pk_fma_f32 v[32:33], v[82:83], v[28:29], v[10:11] op_sel_hi:[1,0,1]
	v_pk_fma_f32 v[2:3], v[30:31], v[2:3], v[2:3]
	v_min_f32_e32 v32, 0x40e00000, v32
	v_min_f32_e32 v33, 0x40e00000, v33
	v_pk_mul_f32 v[180:181], v[32:33], s[20:21] op_sel_hi:[1,0]
	v_cvt_pk_fp8_f32 v21, v2, v3 op_sel:[0,0,1]
	v_exp_f32_e32 v180, v180
	v_exp_f32_e32 v181, v181
	v_pk_fma_f32 v[30:31], v[50:51], v[28:29], v[8:9] op_sel_hi:[1,0,1]
	v_pk_add_f32 v[2:3], v[180:181], 1.0 op_sel_hi:[1,0]
	s_nop 0
	v_rcp_f32_e32 v2, v2
	v_rcp_f32_e32 v3, v3
	v_med3_f32 v30, v30, s37, v176
	v_med3_f32 v31, v31, s37, v176
	v_pk_mul_f32 v[2:3], v[32:33], v[2:3]
	v_pk_fma_f32 v[32:33], v[84:85], v[28:29], v[6:7] op_sel_hi:[1,0,1]
	v_pk_fma_f32 v[2:3], v[30:31], v[2:3], v[2:3]
	v_min_f32_e32 v32, 0x40e00000, v32
	v_min_f32_e32 v33, 0x40e00000, v33
	v_pk_mul_f32 v[180:181], v[32:33], s[20:21] op_sel_hi:[1,0]
	v_cvt_pk_fp8_f32 v27, v2, v3
	v_exp_f32_e32 v180, v180
	v_exp_f32_e32 v181, v181
	v_pk_fma_f32 v[28:29], v[52:53], v[28:29], v[4:5] op_sel_hi:[1,0,1]
	v_pk_fma_f32 v[30:31], v[78:79], v[26:27], v[24:25] op_sel_hi:[1,0,1]
	v_med3_f32 v28, v28, s37, v176
	v_pk_add_f32 v[2:3], v[180:181], 1.0 op_sel_hi:[1,0]
	v_med3_f32 v29, v29, s37, v176
	v_rcp_f32_e32 v2, v2
	v_rcp_f32_e32 v3, v3
	v_min_f32_e32 v30, 0x40e00000, v30
	v_min_f32_e32 v31, 0x40e00000, v31
	v_pk_mul_f32 v[2:3], v[32:33], v[2:3]
	s_nop 0
	v_pk_fma_f32 v[2:3], v[28:29], v[2:3], v[2:3]
	v_cvt_pk_fp8_f32 v27, v2, v3 op_sel:[0,0,1]
	s_nop 0
	v_mov_b32_e32 v3, v27
	v_pk_mul_f32 v[32:33], v[30:31], s[20:21] op_sel_hi:[1,0]
	v_mov_b32_e32 v2, v21
	v_exp_f32_e32 v32, v32
	v_exp_f32_e32 v33, v33
	s_mov_b32 s28, 0x24000
	v_lshl_add_u64 v[28:29], v[188:189], 0, s[28:29]
	global_store_dwordx2 v[28:29], v[2:3], off
	v_pk_add_f32 v[2:3], v[32:33], 1.0 op_sel_hi:[1,0]
	v_pk_fma_f32 v[28:29], v[46:47], v[26:27], v[16:17] op_sel_hi:[1,0,1]
	v_rcp_f32_e32 v2, v2
	v_rcp_f32_e32 v3, v3
	v_med3_f32 v28, v28, s37, v176
	v_med3_f32 v29, v29, s37, v176
	v_pk_mul_f32 v[2:3], v[30:31], v[2:3]
	v_pk_fma_f32 v[30:31], v[80:81], v[26:27], v[14:15] op_sel_hi:[1,0,1]
	v_pk_fma_f32 v[2:3], v[28:29], v[2:3], v[2:3]
	v_min_f32_e32 v30, 0x40e00000, v30
	v_min_f32_e32 v31, 0x40e00000, v31
	v_pk_mul_f32 v[32:33], v[30:31], s[20:21] op_sel_hi:[1,0]
	v_cvt_pk_fp8_f32 v21, v2, v3
	v_exp_f32_e32 v32, v32
	v_exp_f32_e32 v33, v33
	v_pk_fma_f32 v[28:29], v[48:49], v[26:27], v[12:13] op_sel_hi:[1,0,1]
	v_med3_f32 v28, v28, s37, v176
	v_pk_add_f32 v[2:3], v[32:33], 1.0 op_sel_hi:[1,0]
	v_med3_f32 v29, v29, s37, v176
	v_rcp_f32_e32 v2, v2
	v_rcp_f32_e32 v3, v3
	s_nop 0
	v_pk_mul_f32 v[2:3], v[30:31], v[2:3]
	v_pk_fma_f32 v[30:31], v[74:75], v[26:27], v[10:11] op_sel_hi:[1,0,1]
	v_pk_fma_f32 v[2:3], v[28:29], v[2:3], v[2:3]
	v_min_f32_e32 v30, 0x40e00000, v30
	v_min_f32_e32 v31, 0x40e00000, v31
	v_pk_mul_f32 v[32:33], v[30:31], s[20:21] op_sel_hi:[1,0]
	v_cvt_pk_fp8_f32 v21, v2, v3 op_sel:[0,0,1]
	v_exp_f32_e32 v32, v32
	v_exp_f32_e32 v33, v33
	v_pk_fma_f32 v[28:29], v[42:43], v[26:27], v[8:9] op_sel_hi:[1,0,1]
	v_pk_fma_f32 v[24:25], v[70:71], v[22:23], v[24:25] op_sel_hi:[1,0,1]
	v_med3_f32 v28, v28, s37, v176
	v_pk_add_f32 v[2:3], v[32:33], 1.0 op_sel_hi:[1,0]
	v_med3_f32 v29, v29, s37, v176
	v_rcp_f32_e32 v2, v2
	v_rcp_f32_e32 v3, v3
	v_min_f32_e32 v24, 0x40e00000, v24
	v_min_f32_e32 v25, 0x40e00000, v25
	v_pk_fma_f32 v[14:15], v[72:73], v[22:23], v[14:15] op_sel_hi:[1,0,1]
	v_pk_mul_f32 v[2:3], v[30:31], v[2:3]
	v_pk_fma_f32 v[30:31], v[76:77], v[26:27], v[6:7] op_sel_hi:[1,0,1]
	v_pk_fma_f32 v[2:3], v[28:29], v[2:3], v[2:3]
	v_min_f32_e32 v30, 0x40e00000, v30
	v_min_f32_e32 v31, 0x40e00000, v31
	v_pk_mul_f32 v[32:33], v[30:31], s[20:21] op_sel_hi:[1,0]
	v_exp_f32_e32 v32, v32
	v_exp_f32_e32 v33, v33
	v_cvt_pk_fp8_f32 v28, v2, v3
	v_pk_fma_f32 v[26:27], v[44:45], v[26:27], v[4:5] op_sel_hi:[1,0,1]
	v_min_f32_e32 v14, 0x40e00000, v14
	v_pk_add_f32 v[2:3], v[32:33], 1.0 op_sel_hi:[1,0]
	v_med3_f32 v26, v26, s37, v176
	v_rcp_f32_e32 v2, v2
	v_rcp_f32_e32 v3, v3
	v_med3_f32 v27, v27, s37, v176
	v_min_f32_e32 v15, 0x40e00000, v15
	v_pk_fma_f32 v[16:17], v[38:39], v[22:23], v[16:17] op_sel_hi:[1,0,1]
	v_pk_mul_f32 v[2:3], v[30:31], v[2:3]
	v_med3_f32 v16, v16, s37, v176
	v_pk_fma_f32 v[2:3], v[26:27], v[2:3], v[2:3]
	v_cvt_pk_fp8_f32 v28, v2, v3 op_sel:[0,0,1]
	s_nop 0
	v_mov_b32_e32 v3, v28
	v_pk_mul_f32 v[28:29], v[24:25], s[20:21] op_sel_hi:[1,0]
	v_mov_b32_e32 v2, v21
	v_exp_f32_e32 v28, v28
	v_exp_f32_e32 v29, v29
	s_mov_b32 s28, 0x28000
	v_lshl_add_u64 v[26:27], v[188:189], 0, s[28:29]
	global_store_dwordx2 v[26:27], v[2:3], off
	v_pk_add_f32 v[2:3], v[28:29], 1.0 op_sel_hi:[1,0]
	v_med3_f32 v17, v17, s37, v176
	v_rcp_f32_e32 v2, v2
	v_rcp_f32_e32 v3, v3
	v_pk_fma_f32 v[10:11], v[66:67], v[22:23], v[10:11] op_sel_hi:[1,0,1]
	v_pk_fma_f32 v[12:13], v[40:41], v[22:23], v[12:13] op_sel_hi:[1,0,1]
	v_min_f32_e32 v10, 0x40e00000, v10
	v_pk_mul_f32 v[2:3], v[24:25], v[2:3]
	v_pk_mul_f32 v[24:25], v[14:15], s[20:21] op_sel_hi:[1,0]
	v_pk_fma_f32 v[2:3], v[16:17], v[2:3], v[2:3]
	v_exp_f32_e32 v24, v24
	v_exp_f32_e32 v25, v25
	v_cvt_pk_fp8_f32 v16, v2, v3
	v_min_f32_e32 v11, 0x40e00000, v11
	v_pk_add_f32 v[2:3], v[24:25], 1.0 op_sel_hi:[1,0]
	v_med3_f32 v12, v12, s37, v176
	v_rcp_f32_e32 v2, v2
	v_rcp_f32_e32 v3, v3
	v_med3_f32 v13, v13, s37, v176
	v_pk_fma_f32 v[6:7], v[68:69], v[22:23], v[6:7] op_sel_hi:[1,0,1]
	v_pk_fma_f32 v[8:9], v[34:35], v[22:23], v[8:9] op_sel_hi:[1,0,1]
	v_pk_mul_f32 v[2:3], v[14:15], v[2:3]
	v_pk_mul_f32 v[14:15], v[10:11], s[20:21] op_sel_hi:[1,0]
	v_pk_fma_f32 v[2:3], v[12:13], v[2:3], v[2:3]
	v_exp_f32_e32 v14, v14
	v_exp_f32_e32 v15, v15
	v_cvt_pk_fp8_f32 v16, v2, v3 op_sel:[0,0,1]
	v_min_f32_e32 v6, 0x40e00000, v6
	v_pk_add_f32 v[2:3], v[14:15], 1.0 op_sel_hi:[1,0]
	v_min_f32_e32 v7, 0x40e00000, v7
	v_rcp_f32_e32 v2, v2
	v_rcp_f32_e32 v3, v3
	v_med3_f32 v8, v8, s37, v176
	v_med3_f32 v9, v9, s37, v176
	v_pk_fma_f32 v[4:5], v[36:37], v[22:23], v[4:5] op_sel_hi:[1,0,1]
	v_pk_mul_f32 v[2:3], v[10:11], v[2:3]
	v_pk_mul_f32 v[10:11], v[6:7], s[20:21] op_sel_hi:[1,0]
	v_pk_fma_f32 v[2:3], v[8:9], v[2:3], v[2:3]
	v_exp_f32_e32 v10, v10
	v_exp_f32_e32 v11, v11
	v_cvt_pk_fp8_f32 v8, v2, v3
	v_med3_f32 v4, v4, s37, v176
	v_pk_add_f32 v[2:3], v[10:11], 1.0 op_sel_hi:[1,0]
	v_med3_f32 v5, v5, s37, v176
	v_rcp_f32_e32 v2, v2
	v_rcp_f32_e32 v3, v3
	s_nop 0
	v_pk_mul_f32 v[2:3], v[6:7], v[2:3]
	s_nop 0
	v_pk_fma_f32 v[2:3], v[4:5], v[2:3], v[2:3]
	v_cvt_pk_fp8_f32 v8, v2, v3 op_sel:[0,0,1]
	s_nop 0
	v_mov_b32_e32 v3, v8
	v_mov_b32_e32 v2, v16
	s_mov_b32 s28, 0x2c000
	v_lshl_add_u64 v[4:5], v[188:189], 0, s[28:29]
	global_store_dwordx2 v[4:5], v[2:3], off
	s_cbranch_vccnz .LBB0_1920
	s_andn2_b64 vcc, exec, s[0:1]
	s_cbranch_vccnz .LBB0_1919
	s_barrier

.LBB0_2094:
.LBB0_2096:
	v_mov_b32_e32 v2, v166
	v_mov_b32_e32 v3, v165
	v_mov_b32_e32 v4, s39
	ds_read_b32 v4, v4 offset:288
	s_lshl_b32 s15, s85, 11
	v_lshlrev_b32_e32 v18, 3, v2
	s_add_i32 s15, s15, 0
	s_add_i32 s15, s15, 0x21000
	v_add_u32_e32 v2, s66, v18
	v_lshl_add_u32 v8, v2, 2, s15
	ds_read_b128 v[10:13], v8
	s_waitcnt lgkmcnt(1)
	v_readfirstlane_b32 s17, v4
	s_lshl_b32 s17, s17, 2
	s_add_i32 s17, s17, 0
	s_add_i32 s17, s17, 0x201c0
	v_mov_b32_e32 v2, s17
	ds_read2_b32 v[6:7], v2 offset1:32
	v_add_u32_e32 v19, s29, v3
	v_add_u32_e32 v21, 16, v19
	v_add_u32_e32 v23, 32, v19
	v_lshl_add_u32 v22, v21, 2, s15
	s_waitcnt lgkmcnt(0)
	v_readfirstlane_b32 s17, v7
	s_sub_i32 s17, s22, s17
	v_readfirstlane_b32 s26, v6
	v_lshl_add_u32 v6, v19, 2, s15
	v_lshl_add_u32 v24, v23, 2, s15
	ds_read_b128 v[14:17], v8 offset:16
	ds_read_b128 v[2:5], v8 offset:512
	s_lshl_b32 s17, s17, 8
	ds_read_b32 v25, v6 offset:1024
	ds_read_b128 v[6:9], v8 offset:528
	ds_read_b32 v22, v22 offset:1024
	ds_read_b32 v24, v24 offset:1024
	v_add_u32_e32 v20, s17, v19
	v_cmp_gt_i32_e32 vcc, s26, v20
	v_add_u32_e32 v20, s17, v21
	v_add_u32_e32 v27, 0xa0, v19
	s_waitcnt lgkmcnt(3)
	v_cndmask_b32_e32 v176, 0, v25, vcc
	v_cmp_gt_i32_e32 vcc, s26, v20
	v_add_u32_e32 v20, s17, v23
	v_add_u32_e32 v29, 0xb0, v19
	s_waitcnt lgkmcnt(1)
	v_cndmask_b32_e32 v178, 0, v22, vcc
	v_cmp_gt_i32_e32 vcc, s26, v20
	v_add_u32_e32 v20, 48, v19
	v_add_u32_e32 v22, 0x80, v19
	s_waitcnt lgkmcnt(0)
	v_cndmask_b32_e32 v32, 0, v24, vcc
	v_add_u32_e32 v24, 0x90, v19
	v_lshl_add_u32 v21, v20, 2, s15
	v_add_u32_e32 v20, s17, v20
	v_lshl_add_u32 v23, v22, 2, s15
	v_lshl_add_u32 v25, v24, 2, s15
	v_lshl_add_u32 v26, v27, 2, s15
	v_lshl_add_u32 v28, v29, 2, s15
	ds_read_b32 v21, v21 offset:1024
	ds_read_b32 v23, v23 offset:1024
	ds_read_b32 v25, v25 offset:1024
	ds_read_b32 v31, v26 offset:1024
	ds_read_b32 v33, v28 offset:1024
	v_cmp_gt_i32_e32 vcc, s26, v20
	v_add_u32_e32 v20, s17, v22
	v_mul_f32_e32 v180, 0x3b800000, v176
	s_waitcnt lgkmcnt(4)
	v_cndmask_b32_e32 v30, 0, v21, vcc
	v_cmp_gt_i32_e32 vcc, s26, v20
	v_lshl_add_u32 v22, s22, 8, v19
	v_pk_mul_f32 v[158:159], v[158:159], v[180:181] op_sel_hi:[1,0]
	s_waitcnt lgkmcnt(3)
	v_cndmask_b32_e32 v28, 0, v23, vcc
	v_add_u32_e32 v20, s17, v24
	v_ashrrev_i32_e32 v23, 31, v22
	v_pk_fma_f32 v[158:159], v[10:11], v[176:177], v[158:159] op_sel_hi:[1,0,1]
	v_pk_mul_f32 v[154:155], v[154:155], v[180:181] op_sel_hi:[1,0]
	v_cmp_gt_i32_e32 vcc, s26, v20
	v_lshlrev_b64 v[182:183], 10, v[22:23]
	v_pk_fma_f32 v[154:155], v[14:15], v[176:177], v[154:155] op_sel_hi:[1,0,1]
	v_med3_f32 v21, v158, s83, v173
	v_med3_f32 v23, v159, s83, v173
	v_mov_b32_e32 v158, 0
	s_waitcnt lgkmcnt(2)
	v_cndmask_b32_e32 v26, 0, v25, vcc
	v_add_u32_e32 v20, s17, v27
	v_cvt_pk_fp8_f32 v158, v21, v23
	v_med3_f32 v25, v154, s83, v173
	v_med3_f32 v27, v155, s83, v173
	v_mov_b32_e32 v159, 0
	v_pk_mul_f32 v[160:161], v[160:161], v[180:181] op_sel_hi:[1,0]
	v_cvt_pk_fp8_f32 v159, v25, v27
	v_pk_fma_f32 v[160:161], v[12:13], v[176:177], v[160:161] op_sel_hi:[1,0,1]
	v_pk_mul_f32 v[156:157], v[156:157], v[180:181] op_sel_hi:[1,0]
	v_med3_f32 v21, v160, s83, v173
	v_pk_fma_f32 v[156:157], v[16:17], v[176:177], v[156:157] op_sel_hi:[1,0,1]
	v_med3_f32 v23, v161, s83, v173
	v_pk_mul_f32 v[150:151], v[150:151], v[180:181] op_sel_hi:[1,0]
	v_cvt_pk_fp8_f32 v158, v21, v23 op_sel:[0,0,1]
	v_med3_f32 v21, v156, s83, v173
	v_med3_f32 v23, v157, s83, v173
	v_pk_fma_f32 v[150:151], v[2:3], v[176:177], v[150:151] op_sel_hi:[1,0,1]
	v_pk_mul_f32 v[146:147], v[146:147], v[180:181] op_sel_hi:[1,0]
	v_cvt_pk_fp8_f32 v159, v21, v23 op_sel:[0,0,1]
	v_pk_fma_f32 v[146:147], v[6:7], v[176:177], v[146:147] op_sel_hi:[1,0,1]
	v_med3_f32 v21, v150, s83, v173
	v_med3_f32 v23, v151, s83, v173
	v_mov_b32_e32 v150, 0
	v_cvt_pk_fp8_f32 v150, v21, v23
	v_med3_f32 v25, v146, s83, v173
	v_med3_f32 v27, v147, s83, v173
	v_mov_b32_e32 v151, 0
	v_pk_mul_f32 v[152:153], v[152:153], v[180:181] op_sel_hi:[1,0]
	v_cvt_pk_fp8_f32 v151, v25, v27
	v_pk_fma_f32 v[152:153], v[4:5], v[176:177], v[152:153] op_sel_hi:[1,0,1]
	v_pk_mul_f32 v[148:149], v[148:149], v[180:181] op_sel_hi:[1,0]
	v_med3_f32 v21, v152, s83, v173
	v_pk_fma_f32 v[148:149], v[8:9], v[176:177], v[148:149] op_sel_hi:[1,0,1]
	v_med3_f32 v23, v153, s83, v173
	s_or_b32 s27, s38, s66
	v_cvt_pk_fp8_f32 v150, v21, v23 op_sel:[0,0,1]
	v_med3_f32 v21, v148, s83, v173
	v_med3_f32 v23, v149, s83, v173
	v_add_u32_e32 v18, s27, v18
	v_cvt_pk_fp8_f32 v151, v21, v23 op_sel:[0,0,1]
	v_ashrrev_i32_e32 v19, 31, v18
	v_lshl_add_u64 v[146:147], s[10:11], 0, v[182:183]
	v_lshl_add_u64 v[146:147], v[146:147], 0, v[18:19]
	global_store_dwordx2 v[146:147], v[158:159], off
	global_store_dwordx2 v[146:147], v[150:151], off offset:128
	v_mul_f32_e32 v146, 0x3b800000, v178
	v_pk_mul_f32 v[142:143], v[142:143], v[146:147] op_sel_hi:[1,0]
	v_pk_mul_f32 v[138:139], v[138:139], v[146:147] op_sel_hi:[1,0]
	v_pk_fma_f32 v[142:143], v[10:11], v[178:179], v[142:143] op_sel_hi:[1,0,1]
	v_pk_fma_f32 v[138:139], v[14:15], v[178:179], v[138:139] op_sel_hi:[1,0,1]
	v_med3_f32 v21, v142, s83, v173
	v_med3_f32 v23, v143, s83, v173
	v_mov_b32_e32 v142, 0
	v_cvt_pk_fp8_f32 v142, v21, v23
	v_med3_f32 v25, v138, s83, v173
	v_med3_f32 v27, v139, s83, v173
	v_mov_b32_e32 v143, 0
	v_pk_mul_f32 v[144:145], v[144:145], v[146:147] op_sel_hi:[1,0]
	v_cvt_pk_fp8_f32 v143, v25, v27
	v_pk_fma_f32 v[144:145], v[12:13], v[178:179], v[144:145] op_sel_hi:[1,0,1]
	v_pk_mul_f32 v[140:141], v[140:141], v[146:147] op_sel_hi:[1,0]
	v_med3_f32 v21, v144, s83, v173
	v_pk_fma_f32 v[140:141], v[16:17], v[178:179], v[140:141] op_sel_hi:[1,0,1]
	v_med3_f32 v23, v145, s83, v173
	v_pk_mul_f32 v[134:135], v[134:135], v[146:147] op_sel_hi:[1,0]
	v_cvt_pk_fp8_f32 v142, v21, v23 op_sel:[0,0,1]
	v_med3_f32 v21, v140, s83, v173
	v_med3_f32 v23, v141, s83, v173
	v_pk_fma_f32 v[134:135], v[2:3], v[178:179], v[134:135] op_sel_hi:[1,0,1]
	v_pk_mul_f32 v[130:131], v[130:131], v[146:147] op_sel_hi:[1,0]
	v_cvt_pk_fp8_f32 v143, v21, v23 op_sel:[0,0,1]
	v_pk_fma_f32 v[130:131], v[6:7], v[178:179], v[130:131] op_sel_hi:[1,0,1]
	v_med3_f32 v21, v134, s83, v173
	v_med3_f32 v23, v135, s83, v173
	v_mov_b32_e32 v134, 0
	v_cvt_pk_fp8_f32 v134, v21, v23
	v_med3_f32 v25, v130, s83, v173
	v_med3_f32 v27, v131, s83, v173
	v_mov_b32_e32 v135, 0
	v_pk_mul_f32 v[136:137], v[136:137], v[146:147] op_sel_hi:[1,0]
	v_cvt_pk_fp8_f32 v135, v25, v27
	v_pk_fma_f32 v[136:137], v[4:5], v[178:179], v[136:137] op_sel_hi:[1,0,1]
	v_pk_mul_f32 v[132:133], v[132:133], v[146:147] op_sel_hi:[1,0]
	v_add_u32_e32 v148, 16, v22
	v_pk_fma_f32 v[132:133], v[8:9], v[178:179], v[132:133] op_sel_hi:[1,0,1]
	v_med3_f32 v21, v136, s83, v173
	v_med3_f32 v23, v137, s83, v173
	v_ashrrev_i32_e32 v149, 31, v148
	v_cvt_pk_fp8_f32 v134, v21, v23 op_sel:[0,0,1]
	v_med3_f32 v21, v132, s83, v173
	v_med3_f32 v23, v133, s83, v173
	v_lshlrev_b64 v[148:149], 10, v[148:149]
	v_cvt_pk_fp8_f32 v135, v21, v23 op_sel:[0,0,1]
	v_lshl_add_u64 v[130:131], s[10:11], 0, v[148:149]
	v_lshl_add_u64 v[130:131], v[130:131], 0, v[18:19]
	global_store_dwordx2 v[130:131], v[142:143], off
	global_store_dwordx2 v[130:131], v[134:135], off offset:128
	v_mul_f32_e32 v130, 0x3b800000, v32
	v_pk_mul_f32 v[126:127], v[126:127], v[130:131] op_sel_hi:[1,0]
	v_pk_mul_f32 v[122:123], v[122:123], v[130:131] op_sel_hi:[1,0]
	s_waitcnt lgkmcnt(0)
	v_pk_fma_f32 v[126:127], v[10:11], v[32:33], v[126:127] op_sel_hi:[1,0,1]
	v_pk_fma_f32 v[122:123], v[14:15], v[32:33], v[122:123] op_sel_hi:[1,0,1]
	v_med3_f32 v21, v126, s83, v173
	v_med3_f32 v23, v127, s83, v173
	v_mov_b32_e32 v126, 0
	v_cvt_pk_fp8_f32 v126, v21, v23
	v_med3_f32 v25, v122, s83, v173
	v_med3_f32 v27, v123, s83, v173
	v_mov_b32_e32 v127, 0
	v_pk_mul_f32 v[128:129], v[128:129], v[130:131] op_sel_hi:[1,0]
	v_cvt_pk_fp8_f32 v127, v25, v27
	v_pk_fma_f32 v[128:129], v[12:13], v[32:33], v[128:129] op_sel_hi:[1,0,1]
	v_pk_mul_f32 v[124:125], v[124:125], v[130:131] op_sel_hi:[1,0]
	v_cmp_gt_i32_e32 vcc, s26, v20
	v_add_u32_e32 v20, s17, v29
	v_pk_fma_f32 v[124:125], v[16:17], v[32:33], v[124:125] op_sel_hi:[1,0,1]
	v_med3_f32 v21, v128, s83, v173
	v_med3_f32 v23, v129, s83, v173
	v_pk_mul_f32 v[118:119], v[118:119], v[130:131] op_sel_hi:[1,0]
	v_cndmask_b32_e32 v24, 0, v31, vcc
	v_cmp_gt_i32_e32 vcc, s26, v20
	v_cvt_pk_fp8_f32 v126, v21, v23 op_sel:[0,0,1]
	v_med3_f32 v21, v124, s83, v173
	v_med3_f32 v23, v125, s83, v173
	v_pk_mul_f32 v[120:121], v[120:121], v[130:131] op_sel_hi:[1,0]
	v_pk_fma_f32 v[118:119], v[2:3], v[32:33], v[118:119] op_sel_hi:[1,0,1]
	v_pk_mul_f32 v[114:115], v[114:115], v[130:131] op_sel_hi:[1,0]
	v_pk_mul_f32 v[116:117], v[116:117], v[130:131] op_sel_hi:[1,0]
	v_cndmask_b32_e32 v20, 0, v33, vcc
	v_cvt_pk_fp8_f32 v127, v21, v23 op_sel:[0,0,1]
	v_pk_fma_f32 v[120:121], v[4:5], v[32:33], v[120:121] op_sel_hi:[1,0,1]
	v_pk_fma_f32 v[116:117], v[8:9], v[32:33], v[116:117] op_sel_hi:[1,0,1]
	v_pk_fma_f32 v[32:33], v[6:7], v[32:33], v[114:115] op_sel_hi:[1,0,1]
	v_med3_f32 v21, v118, s83, v173
	v_med3_f32 v23, v119, s83, v173
	v_mov_b32_e32 v114, 0
	v_cvt_pk_fp8_f32 v114, v21, v23
	v_med3_f32 v25, v32, s83, v173
	v_med3_f32 v27, v33, s83, v173
	v_mov_b32_e32 v115, 0
	v_cvt_pk_fp8_f32 v115, v25, v27
	v_add_u32_e32 v132, 32, v22
	v_med3_f32 v21, v120, s83, v173
	v_med3_f32 v23, v121, s83, v173
	v_ashrrev_i32_e32 v133, 31, v132
	v_cvt_pk_fp8_f32 v114, v21, v23 op_sel:[0,0,1]
	v_med3_f32 v21, v116, s83, v173
	v_med3_f32 v23, v117, s83, v173
	v_lshlrev_b64 v[132:133], 10, v[132:133]
	v_cvt_pk_fp8_f32 v115, v21, v23 op_sel:[0,0,1]
	v_lshl_add_u64 v[32:33], s[10:11], 0, v[132:133]
	v_lshl_add_u64 v[32:33], v[32:33], 0, v[18:19]
	global_store_dwordx2 v[32:33], v[126:127], off
	global_store_dwordx2 v[32:33], v[114:115], off offset:128
	v_mul_f32_e32 v32, 0x3b800000, v30
	v_pk_mul_f32 v[110:111], v[110:111], v[32:33] op_sel_hi:[1,0]
	v_pk_mul_f32 v[106:107], v[106:107], v[32:33] op_sel_hi:[1,0]
	v_pk_fma_f32 v[110:111], v[10:11], v[30:31], v[110:111] op_sel_hi:[1,0,1]
	v_pk_fma_f32 v[106:107], v[14:15], v[30:31], v[106:107] op_sel_hi:[1,0,1]
	v_med3_f32 v21, v110, s83, v173
	v_med3_f32 v23, v111, s83, v173
	v_mov_b32_e32 v110, 0
	v_cvt_pk_fp8_f32 v110, v21, v23
	v_med3_f32 v25, v106, s83, v173
	v_med3_f32 v27, v107, s83, v173
	v_mov_b32_e32 v111, 0
	v_pk_mul_f32 v[112:113], v[112:113], v[32:33] op_sel_hi:[1,0]
	v_cvt_pk_fp8_f32 v111, v25, v27
	v_pk_fma_f32 v[112:113], v[12:13], v[30:31], v[112:113] op_sel_hi:[1,0,1]
	v_pk_mul_f32 v[108:109], v[108:109], v[32:33] op_sel_hi:[1,0]
	v_med3_f32 v21, v112, s83, v173
	v_pk_fma_f32 v[108:109], v[16:17], v[30:31], v[108:109] op_sel_hi:[1,0,1]
	v_med3_f32 v23, v113, s83, v173
	v_pk_mul_f32 v[102:103], v[102:103], v[32:33] op_sel_hi:[1,0]
	v_cvt_pk_fp8_f32 v110, v21, v23 op_sel:[0,0,1]
	v_med3_f32 v21, v108, s83, v173
	v_med3_f32 v23, v109, s83, v173
	v_pk_mul_f32 v[104:105], v[104:105], v[32:33] op_sel_hi:[1,0]
	v_pk_fma_f32 v[102:103], v[2:3], v[30:31], v[102:103] op_sel_hi:[1,0,1]
	v_pk_mul_f32 v[98:99], v[98:99], v[32:33] op_sel_hi:[1,0]
	v_pk_mul_f32 v[32:33], v[100:101], v[32:33] op_sel_hi:[1,0]
	v_cvt_pk_fp8_f32 v111, v21, v23 op_sel:[0,0,1]
	v_pk_fma_f32 v[104:105], v[4:5], v[30:31], v[104:105] op_sel_hi:[1,0,1]
	v_pk_fma_f32 v[32:33], v[8:9], v[30:31], v[32:33] op_sel_hi:[1,0,1]
	v_pk_fma_f32 v[30:31], v[6:7], v[30:31], v[98:99] op_sel_hi:[1,0,1]
	v_med3_f32 v21, v102, s83, v173
	v_med3_f32 v23, v103, s83, v173
	v_mov_b32_e32 v98, 0
	v_cvt_pk_fp8_f32 v98, v21, v23
	v_med3_f32 v25, v30, s83, v173
	v_med3_f32 v27, v31, s83, v173
	v_mov_b32_e32 v99, 0
	v_med3_f32 v21, v104, s83, v173
	v_med3_f32 v23, v105, s83, v173
	v_cvt_pk_fp8_f32 v99, v25, v27
	v_cvt_pk_fp8_f32 v98, v21, v23 op_sel:[0,0,1]
	v_med3_f32 v21, v32, s83, v173
	v_mul_f32_e32 v32, 0x3b800000, v28
	v_pk_mul_f32 v[94:95], v[94:95], v[32:33] op_sel_hi:[1,0]
	v_med3_f32 v23, v33, s83, v173
	v_pk_fma_f32 v[94:95], v[10:11], v[28:29], v[94:95] op_sel_hi:[1,0,1]
	v_pk_mul_f32 v[90:91], v[90:91], v[32:33] op_sel_hi:[1,0]
	v_cvt_pk_fp8_f32 v99, v21, v23 op_sel:[0,0,1]
	v_pk_fma_f32 v[90:91], v[14:15], v[28:29], v[90:91] op_sel_hi:[1,0,1]
	v_med3_f32 v21, v94, s83, v173
	v_med3_f32 v23, v95, s83, v173
	v_mov_b32_e32 v94, 0
	v_cvt_pk_fp8_f32 v94, v21, v23
	v_med3_f32 v25, v90, s83, v173
	v_med3_f32 v27, v91, s83, v173
	v_mov_b32_e32 v95, 0
	v_pk_mul_f32 v[96:97], v[96:97], v[32:33] op_sel_hi:[1,0]
	v_cvt_pk_fp8_f32 v95, v25, v27
	v_pk_fma_f32 v[96:97], v[12:13], v[28:29], v[96:97] op_sel_hi:[1,0,1]
	v_pk_mul_f32 v[92:93], v[92:93], v[32:33] op_sel_hi:[1,0]
	v_med3_f32 v21, v96, s83, v173
	v_pk_fma_f32 v[92:93], v[16:17], v[28:29], v[92:93] op_sel_hi:[1,0,1]
	v_med3_f32 v23, v97, s83, v173
	v_pk_mul_f32 v[86:87], v[86:87], v[32:33] op_sel_hi:[1,0]
	v_add_u32_e32 v114, 48, v22
	v_cvt_pk_fp8_f32 v94, v21, v23 op_sel:[0,0,1]
	v_med3_f32 v21, v92, s83, v173
	v_med3_f32 v23, v93, s83, v173
	v_pk_mul_f32 v[88:89], v[88:89], v[32:33] op_sel_hi:[1,0]
	v_pk_fma_f32 v[86:87], v[2:3], v[28:29], v[86:87] op_sel_hi:[1,0,1]
	v_pk_mul_f32 v[82:83], v[82:83], v[32:33] op_sel_hi:[1,0]
	v_pk_mul_f32 v[32:33], v[84:85], v[32:33] op_sel_hi:[1,0]
	v_ashrrev_i32_e32 v115, 31, v114
	v_cvt_pk_fp8_f32 v95, v21, v23 op_sel:[0,0,1]
	v_pk_fma_f32 v[88:89], v[4:5], v[28:29], v[88:89] op_sel_hi:[1,0,1]
	v_pk_fma_f32 v[32:33], v[8:9], v[28:29], v[32:33] op_sel_hi:[1,0,1]
	v_pk_fma_f32 v[28:29], v[6:7], v[28:29], v[82:83] op_sel_hi:[1,0,1]
	v_med3_f32 v21, v86, s83, v173
	v_med3_f32 v23, v87, s83, v173
	v_mov_b32_e32 v82, 0
	v_lshlrev_b64 v[114:115], 10, v[114:115]
	v_cvt_pk_fp8_f32 v82, v21, v23
	v_med3_f32 v25, v28, s83, v173
	v_med3_f32 v27, v29, s83, v173
	v_mov_b32_e32 v83, 0
	v_lshl_add_u64 v[30:31], s[10:11], 0, v[114:115]
	v_cvt_pk_fp8_f32 v83, v25, v27
	v_lshl_add_u64 v[30:31], v[30:31], 0, v[18:19]
	global_store_dwordx2 v[30:31], v[110:111], off
	global_store_dwordx2 v[30:31], v[98:99], off offset:128
	v_add_u32_e32 v30, 0x80, v22
	v_med3_f32 v21, v88, s83, v173
	v_med3_f32 v23, v89, s83, v173
	v_ashrrev_i32_e32 v31, 31, v30
	v_cvt_pk_fp8_f32 v82, v21, v23 op_sel:[0,0,1]
	v_med3_f32 v21, v32, s83, v173
	v_med3_f32 v23, v33, s83, v173
	v_lshlrev_b64 v[30:31], 10, v[30:31]
	v_cvt_pk_fp8_f32 v83, v21, v23 op_sel:[0,0,1]
	v_lshl_add_u64 v[28:29], s[10:11], 0, v[30:31]
	v_lshl_add_u64 v[28:29], v[28:29], 0, v[18:19]
	global_store_dwordx2 v[28:29], v[94:95], off
	global_store_dwordx2 v[28:29], v[82:83], off offset:128
	v_mul_f32_e32 v28, 0x3b800000, v26
	v_pk_mul_f32 v[32:33], v[78:79], v[28:29] op_sel_hi:[1,0]
	v_pk_mul_f32 v[74:75], v[74:75], v[28:29] op_sel_hi:[1,0]
	v_pk_fma_f32 v[32:33], v[10:11], v[26:27], v[32:33] op_sel_hi:[1,0,1]
	v_pk_mul_f32 v[78:79], v[80:81], v[28:29] op_sel_hi:[1,0]
	v_pk_mul_f32 v[76:77], v[76:77], v[28:29] op_sel_hi:[1,0]
	v_pk_fma_f32 v[74:75], v[14:15], v[26:27], v[74:75] op_sel_hi:[1,0,1]
	v_med3_f32 v21, v32, s83, v173
	v_med3_f32 v23, v33, s83, v173
	v_mov_b32_e32 v32, 0
	v_pk_fma_f32 v[78:79], v[12:13], v[26:27], v[78:79] op_sel_hi:[1,0,1]
	v_pk_fma_f32 v[76:77], v[16:17], v[26:27], v[76:77] op_sel_hi:[1,0,1]
	v_cvt_pk_fp8_f32 v32, v21, v23
	v_med3_f32 v25, v74, s83, v173
	v_med3_f32 v27, v75, s83, v173
	v_mov_b32_e32 v33, 0
	v_cvt_pk_fp8_f32 v33, v25, v27
	v_med3_f32 v21, v78, s83, v173
	v_med3_f32 v23, v79, s83, v173
	v_pk_mul_f32 v[70:71], v[70:71], v[28:29] op_sel_hi:[1,0]
	v_cvt_pk_fp8_f32 v32, v21, v23 op_sel:[0,0,1]
	v_med3_f32 v21, v76, s83, v173
	v_med3_f32 v23, v77, s83, v173
	v_pk_mul_f32 v[72:73], v[72:73], v[28:29] op_sel_hi:[1,0]
	v_pk_fma_f32 v[70:71], v[2:3], v[26:27], v[70:71] op_sel_hi:[1,0,1]
	v_pk_mul_f32 v[66:67], v[66:67], v[28:29] op_sel_hi:[1,0]
	v_pk_mul_f32 v[28:29], v[68:69], v[28:29] op_sel_hi:[1,0]
	v_cvt_pk_fp8_f32 v33, v21, v23 op_sel:[0,0,1]
	v_pk_fma_f32 v[72:73], v[4:5], v[26:27], v[72:73] op_sel_hi:[1,0,1]
	v_pk_fma_f32 v[28:29], v[8:9], v[26:27], v[28:29] op_sel_hi:[1,0,1]
	v_pk_fma_f32 v[26:27], v[6:7], v[26:27], v[66:67] op_sel_hi:[1,0,1]
	v_med3_f32 v21, v70, s83, v173
	v_med3_f32 v23, v71, s83, v173
	v_mov_b32_e32 v66, 0
	v_cvt_pk_fp8_f32 v66, v21, v23
	v_med3_f32 v25, v26, s83, v173
	v_med3_f32 v26, v27, s83, v173
	v_mov_b32_e32 v67, 0
	v_cvt_pk_fp8_f32 v67, v25, v26
	v_add_u32_e32 v30, 0x90, v22
	v_med3_f32 v21, v72, s83, v173
	v_med3_f32 v23, v73, s83, v173
	v_ashrrev_i32_e32 v31, 31, v30
	v_cvt_pk_fp8_f32 v66, v21, v23 op_sel:[0,0,1]
	v_med3_f32 v21, v28, s83, v173
	v_med3_f32 v23, v29, s83, v173
	v_lshlrev_b64 v[30:31], 10, v[30:31]
	v_cvt_pk_fp8_f32 v67, v21, v23 op_sel:[0,0,1]
	v_lshl_add_u64 v[26:27], s[10:11], 0, v[30:31]
	v_lshl_add_u64 v[26:27], v[26:27], 0, v[18:19]
	global_store_dwordx2 v[26:27], v[32:33], off
	global_store_dwordx2 v[26:27], v[66:67], off offset:128
	v_mul_f32_e32 v26, 0x3b800000, v24
	v_pk_mul_f32 v[30:31], v[62:63], v[26:27] op_sel_hi:[1,0]
	v_pk_mul_f32 v[58:59], v[58:59], v[26:27] op_sel_hi:[1,0]
	v_pk_fma_f32 v[30:31], v[10:11], v[24:25], v[30:31] op_sel_hi:[1,0,1]
	v_pk_mul_f32 v[32:33], v[64:65], v[26:27] op_sel_hi:[1,0]
	v_pk_mul_f32 v[60:61], v[60:61], v[26:27] op_sel_hi:[1,0]
	v_pk_fma_f32 v[58:59], v[14:15], v[24:25], v[58:59] op_sel_hi:[1,0,1]
	v_med3_f32 v21, v30, s83, v173
	v_med3_f32 v23, v31, s83, v173
	v_mov_b32_e32 v30, 0
	v_pk_fma_f32 v[32:33], v[12:13], v[24:25], v[32:33] op_sel_hi:[1,0,1]
	v_pk_fma_f32 v[60:61], v[16:17], v[24:25], v[60:61] op_sel_hi:[1,0,1]
	v_cvt_pk_fp8_f32 v30, v21, v23
	v_med3_f32 v25, v58, s83, v173
	v_med3_f32 v27, v59, s83, v173
	v_mov_b32_e32 v31, 0
	v_cvt_pk_fp8_f32 v31, v25, v27
	v_med3_f32 v21, v32, s83, v173
	v_med3_f32 v23, v33, s83, v173
	v_pk_mul_f32 v[32:33], v[54:55], v[26:27] op_sel_hi:[1,0]
	v_cvt_pk_fp8_f32 v30, v21, v23 op_sel:[0,0,1]
	v_med3_f32 v21, v60, s83, v173
	v_med3_f32 v23, v61, s83, v173
	v_pk_mul_f32 v[54:55], v[56:57], v[26:27] op_sel_hi:[1,0]
	v_pk_fma_f32 v[32:33], v[2:3], v[24:25], v[32:33] op_sel_hi:[1,0,1]
	v_pk_mul_f32 v[50:51], v[50:51], v[26:27] op_sel_hi:[1,0]
	v_pk_mul_f32 v[26:27], v[52:53], v[26:27] op_sel_hi:[1,0]
	v_cvt_pk_fp8_f32 v31, v21, v23 op_sel:[0,0,1]
	v_pk_fma_f32 v[54:55], v[4:5], v[24:25], v[54:55] op_sel_hi:[1,0,1]
	v_pk_fma_f32 v[26:27], v[8:9], v[24:25], v[26:27] op_sel_hi:[1,0,1]
	v_pk_fma_f32 v[24:25], v[6:7], v[24:25], v[50:51] op_sel_hi:[1,0,1]
	v_med3_f32 v21, v32, s83, v173
	v_med3_f32 v23, v33, s83, v173
	v_mov_b32_e32 v32, 0
	v_cvt_pk_fp8_f32 v32, v21, v23
	v_med3_f32 v24, v24, s83, v173
	v_med3_f32 v25, v25, s83, v173
	v_mov_b32_e32 v33, 0
	v_cvt_pk_fp8_f32 v33, v24, v25
	v_add_u32_e32 v28, 0xa0, v22
	v_med3_f32 v21, v54, s83, v173
	v_med3_f32 v23, v55, s83, v173
	v_ashrrev_i32_e32 v29, 31, v28
	v_cvt_pk_fp8_f32 v32, v21, v23 op_sel:[0,0,1]
	v_med3_f32 v21, v26, s83, v173
	v_med3_f32 v23, v27, s83, v173
	v_lshlrev_b64 v[28:29], 10, v[28:29]
	v_cvt_pk_fp8_f32 v33, v21, v23 op_sel:[0,0,1]
	v_lshl_add_u64 v[24:25], s[10:11], 0, v[28:29]
	v_lshl_add_u64 v[24:25], v[24:25], 0, v[18:19]
	global_store_dwordx2 v[24:25], v[30:31], off
	global_store_dwordx2 v[24:25], v[32:33], off offset:128
	v_mul_f32_e32 v24, 0x3b800000, v20
	v_pk_mul_f32 v[26:27], v[46:47], v[24:25] op_sel_hi:[1,0]
	v_pk_mul_f32 v[28:29], v[48:49], v[24:25] op_sel_hi:[1,0]
	v_pk_fma_f32 v[10:11], v[10:11], v[20:21], v[26:27] op_sel_hi:[1,0,1]
	v_pk_fma_f32 v[12:13], v[12:13], v[20:21], v[28:29] op_sel_hi:[1,0,1]
	v_pk_mul_f32 v[26:27], v[42:43], v[24:25] op_sel_hi:[1,0]
	v_pk_mul_f32 v[28:29], v[44:45], v[24:25] op_sel_hi:[1,0]
	v_pk_fma_f32 v[14:15], v[14:15], v[20:21], v[26:27] op_sel_hi:[1,0,1]
	v_pk_fma_f32 v[16:17], v[16:17], v[20:21], v[28:29] op_sel_hi:[1,0,1]
	v_med3_f32 v21, v10, s83, v173
	v_med3_f32 v11, v11, s83, v173
	v_mov_b32_e32 v10, 0
	v_cvt_pk_fp8_f32 v10, v21, v11
	v_med3_f32 v14, v14, s83, v173
	v_med3_f32 v15, v15, s83, v173
	v_mov_b32_e32 v11, 0
	v_cvt_pk_fp8_f32 v11, v14, v15
	v_med3_f32 v12, v12, s83, v173
	v_med3_f32 v13, v13, s83, v173
	v_cvt_pk_fp8_f32 v10, v12, v13 op_sel:[0,0,1]
	v_med3_f32 v12, v16, s83, v173
	v_med3_f32 v13, v17, s83, v173
	v_cvt_pk_fp8_f32 v11, v12, v13 op_sel:[0,0,1]
	v_pk_mul_f32 v[12:13], v[38:39], v[24:25] op_sel_hi:[1,0]
	v_pk_mul_f32 v[14:15], v[40:41], v[24:25] op_sel_hi:[1,0]
	v_pk_fma_f32 v[2:3], v[2:3], v[20:21], v[12:13] op_sel_hi:[1,0,1]
	v_pk_mul_f32 v[12:13], v[34:35], v[24:25] op_sel_hi:[1,0]
	v_med3_f32 v3, v3, s83, v173
	v_pk_fma_f32 v[6:7], v[6:7], v[20:21], v[12:13] op_sel_hi:[1,0,1]
	v_med3_f32 v12, v2, s83, v173
	v_mov_b32_e32 v2, 0
	v_cvt_pk_fp8_f32 v2, v12, v3
	v_med3_f32 v6, v6, s83, v173
	v_med3_f32 v7, v7, s83, v173
	v_mov_b32_e32 v3, 0
	v_cvt_pk_fp8_f32 v3, v6, v7
	v_pk_fma_f32 v[4:5], v[4:5], v[20:21], v[14:15] op_sel_hi:[1,0,1]
	v_pk_mul_f32 v[14:15], v[36:37], v[24:25] op_sel_hi:[1,0]
	v_add_u32_e32 v22, 0xb0, v22
	v_pk_fma_f32 v[8:9], v[8:9], v[20:21], v[14:15] op_sel_hi:[1,0,1]
	v_med3_f32 v4, v4, s83, v173
	v_med3_f32 v5, v5, s83, v173
	v_ashrrev_i32_e32 v23, 31, v22
	v_cvt_pk_fp8_f32 v2, v4, v5 op_sel:[0,0,1]
	v_med3_f32 v4, v8, s83, v173
	v_med3_f32 v5, v9, s83, v173
	v_lshlrev_b64 v[22:23], 10, v[22:23]
	v_cvt_pk_fp8_f32 v3, v4, v5 op_sel:[0,0,1]
	v_lshl_add_u64 v[4:5], s[10:11], 0, v[22:23]
	v_lshl_add_u64 v[4:5], v[4:5], 0, v[18:19]
	s_and_b64 vcc, exec, s[6:7]
	s_mov_b64 s[6:7], -1
	v_readlane_b32 s90, v253, 26
	global_store_dwordx2 v[4:5], v[10:11], off
	global_store_dwordx2 v[4:5], v[2:3], off offset:128
	s_cbranch_vccnz .LBB0_2057
	s_andn2_b64 vcc, exec, s[8:9]
	s_cbranch_vccnz .LBB0_2056
	s_barrier
	s_branch .LBB0_2056
